# GDN section d, kdT-fragment pieces (waves 1-7): ten LDS reads issued together, one wait
# baseline (speedup 1.0000x reference)
.LBB0_333:
	v_add_u32_e32 v12, 0x400, v140
	s_movk_i32 s22, 0x3ff
	v_bfe_u32 v13, v12, 5, 1
	v_cmp_lt_i32_e32 vcc, s22, v12
	v_lshrrev_b32_e32 v14, 2, v12
	s_and_saveexec_b64 s[22:23], vcc
	s_xor_b64 s[22:23], exec, s[22:23]
	s_cbranch_execz .LBB0_335
	v_and_b32_e32 v0, 48, v14
	v_lshl_or_b32 v0, v13, 2, v0
	v_lshrrev_b32_e32 v1, 2, v140
	v_and_b32_e32 v1, 0x3fffffc0, v1
	v_mul_u32_u24_e32 v2, 0x110, v0
	v_add3_u32 v13, v11, v1, v2
	v_lshl_add_u32 v0, v0, 2, 0
	v_add_u32_e32 v6, 0x1c700, v0
	ds_read_u16 v16, v13
	ds_read_u16 v17, v13 offset:272
	ds_read_u16 v18, v13 offset:544
	ds_read_u16 v19, v13 offset:816
	ds_read_u16 v20, v13 offset:2176
	ds_read_u16 v21, v13 offset:2448
	ds_read_u16 v22, v13 offset:2720
	ds_read_u16 v23, v13 offset:2992
	ds_read_b128 v[24:27], v6
	ds_read_b128 v[28:31], v6 offset:32
	s_waitcnt lgkmcnt(0)
	v_lshlrev_b32_e32 v16, 16, v16
	v_lshlrev_b32_e32 v17, 16, v17
	v_lshlrev_b32_e32 v18, 16, v18
	v_lshlrev_b32_e32 v19, 16, v19
	v_lshlrev_b32_e32 v20, 16, v20
	v_lshlrev_b32_e32 v21, 16, v21
	v_lshlrev_b32_e32 v22, 16, v22
	v_lshlrev_b32_e32 v23, 16, v23
	v_mul_f32_e32 v16, v24, v16
	v_mul_f32_e32 v17, v25, v17
	v_mul_f32_e32 v18, v26, v18
	v_mul_f32_e32 v19, v27, v19
	v_mul_f32_e32 v20, v28, v20
	v_mul_f32_e32 v21, v29, v21
	v_mul_f32_e32 v22, v30, v22
	v_mul_f32_e32 v23, v31, v23
	v_cvt_pk_bf16_f32 v0, v16, v17
	v_cvt_pk_bf16_f32 v1, v18, v19
	v_cvt_pk_bf16_f32 v2, v20, v21
	v_cvt_pk_bf16_f32 v3, v22, v23
	v_mov_b64_e32 v[6:7], v[140:141]
